# v040 + the 64 workgroups without an R2 GEMM unit touch this layer's routed down-projection weights (one dword per 64 B) so the routed-down phase finds them in the memory-side cache
# baseline (speedup 1.0000x reference)
; #define PTRS() Ptrs P; load_ptrs(P); unsigned char* const ws = P.ws; (void)ws
; template <class Epi, class Sched, bool ALIGN_EPI = false, bool SP2 = false, bool FP8 = false>
; __device__ __forceinline__ void gemm_phase(PG8_LAS unsigned char* lds, const Gemm g, const Sched& S, const Epi& E) {
;     ...
;     for (int i = 0; i < 2; ++i) { int R, C; stage_rc(tid * 16 + i * 8192, R, C); const int Rb = Epi::PERM ? ((R & ~31) + perm32(R & 31)) : R;
;         voffA[i] = FP8 ? (unsigned)(R * K + C * 2) : (unsigned)(R * K + C) * 2u; voffB[i] = FP8 ? (unsigned)(Rb * K + C * 2) : (unsigned)(Rb * K + C) * 2u; RA[i] = R; CA[i] = (unsigned)C * 2u; }
;     unsigned vA[2][2], vAn[2][2];
;     const size_t kstep = (size_t)(BK * 2);
;     const size_t hstep = (size_t)HALF * K * (FP8 ? 1 : 2);
;     const size_t tstep = 2 * hstep;
;     const unsigned ldsw = (unsigned)wid * 1024u;
;     const int aoff = lds_byte(wr * 64 + fr, fq * 8), boff = lds_byte(wc * 32 + fr, fq * 8);
; __global__ void __launch_bounds__(NTHR, 2) mk_fwd(Args args) {
;     ...
;         if (EN(9) && IN(k0 + 7)) {
;             PTRS();
;             pg8::Gemm g{(const bf16*)(ws + WS_XM), (const bf16*)(ws + WS_RS + (size_t)layer * RS_L), T, 768, 1024}; pg8::StaticOrder S; S.init(T, 768, G, (int)blockIdx.x);
;             EpiRouterShared E{(float*)(ws + WS_LOGIT), (bf16*)(ws + WS_ACT)}; pg8::gemm_phase<EpiRouterShared, pg8::StaticOrder, GEMM_ALIGN, GEMM_SP2>(lds, g, S, E);
.LBB0_1042:
	s_andn2_b64 vcc, exec, s[0:1]
	s_cbranch_vccnz .LBB0_1117
	v_readlane_b32 s4, v254, 25
	s_mov_b64 s[0:1], s[76:77]
	s_waitcnt vmcnt(0)
	v_mov_b32_e32 v16, v0
	v_readlane_b32 s5, v254, 26
	s_andn2_b64 vcc, exec, s[4:5]
	v_readfirstlane_b32 s4, v16
	s_cbranch_vccz .Lr2_has_unit
	s_load_dwordx2 s[20:21], s[0:1], 0xd8
	v_readlane_b32 s5, v255, 28
	s_nop 3
	s_lshr_b32 s8, s5, 5
	s_and_b32 s9, s5, 31
	s_sub_i32 s9, s9, 24
	s_lshl_b32 s8, s8, 3
	s_add_i32 s8, s8, s9
	s_and_b32 s8, s8, 63
	s_lshl_b32 s8, s8, 19
	s_mul_i32 s9, s86, 0x4080000
	s_waitcnt lgkmcnt(0)
	s_add_u32 s20, s20, s9
	s_addc_u32 s21, s21, 0
	s_add_u32 s20, s20, 0x24100000
	s_addc_u32 s21, s21, 0
	s_add_u32 s20, s20, s8
	s_addc_u32 s21, s21, 0
	v_lshlrev_b32_e32 v1, 6, v16
	global_load_dword v2, v1, s[20:21]
	s_add_u32 s20, s20, 0x8000
	s_addc_u32 s21, s21, 0
	global_load_dword v3, v1, s[20:21]
	s_add_u32 s20, s20, 0x8000
	s_addc_u32 s21, s21, 0
	global_load_dword v4, v1, s[20:21]
	s_add_u32 s20, s20, 0x8000
	s_addc_u32 s21, s21, 0
	global_load_dword v5, v1, s[20:21]
	s_add_u32 s20, s20, 0x8000
	s_addc_u32 s21, s21, 0
	global_load_dword v6, v1, s[20:21]
	s_add_u32 s20, s20, 0x8000
	s_addc_u32 s21, s21, 0
	global_load_dword v7, v1, s[20:21]
	s_add_u32 s20, s20, 0x8000
	s_addc_u32 s21, s21, 0
	global_load_dword v8, v1, s[20:21]
	s_add_u32 s20, s20, 0x8000
	s_addc_u32 s21, s21, 0
	global_load_dword v9, v1, s[20:21]
	s_add_u32 s20, s20, 0x8000
	s_addc_u32 s21, s21, 0
	global_load_dword v10, v1, s[20:21]
	s_add_u32 s20, s20, 0x8000
	s_addc_u32 s21, s21, 0
	global_load_dword v11, v1, s[20:21]
	s_add_u32 s20, s20, 0x8000
	s_addc_u32 s21, s21, 0
	global_load_dword v12, v1, s[20:21]
	s_add_u32 s20, s20, 0x8000
	s_addc_u32 s21, s21, 0
	global_load_dword v13, v1, s[20:21]
	s_add_u32 s20, s20, 0x8000
	s_addc_u32 s21, s21, 0
	global_load_dword v14, v1, s[20:21]
	s_add_u32 s20, s20, 0x8000
	s_addc_u32 s21, s21, 0
	global_load_dword v15, v1, s[20:21]
	s_add_u32 s20, s20, 0x8000
	s_addc_u32 s21, s21, 0
	global_load_dword v16, v1, s[20:21]
	s_add_u32 s20, s20, 0x8000
	s_addc_u32 s21, s21, 0
	global_load_dword v17, v1, s[20:21]
	s_branch .LBB0_1063
.Lr2_has_unit:
	v_lshlrev_b32_e32 v1, 4, v16
	v_add_u32_e32 v2, 0x2000, v1
	v_ashrrev_i32_e32 v3, 31, v2
	v_lshrrev_b32_e32 v3, 22, v3
	v_add_u32_e32 v3, v2, v3
	v_ashrrev_i32_e32 v10, 10, v3
	s_load_dwordx2 s[20:21], s[0:1], 0xd8
	v_mul_i32_i24_e32 v3, 0x400, v10
	v_sub_u32_e32 v2, v2, v3
	v_lshrrev_b32_e32 v3, 4, v2
	v_bitop3_b32 v2, v3, v2, 32 bitop3:0x6c
	v_ashrrev_i32_e32 v3, 31, v2
	s_waitcnt lgkmcnt(0)
	s_add_u32 s11, s20, 0x38600000
	v_lshrrev_b32_e32 v3, 26, v3
	s_mul_i32 s0, s86, 0x180000
	s_addc_u32 s16, s21, 0
	v_add_u32_e32 v3, v2, v3
	v_lshlrev_b32_e32 v4, 3, v10
	s_add_u32 s0, s20, s0
	v_ashrrev_i32_e32 v11, 6, v3
	v_and_b32_e32 v4, -16, v4
	s_addc_u32 s1, s21, 0
	v_add_u32_e32 v4, v11, v4
	s_add_u32 s42, s0, 0x1d00000
	v_and_b32_e32 v5, 3, v11
	s_mov_b32 s0, 0x1fffe0
	v_lshrrev_b32_e32 v6, 2, v4
	v_lshlrev_b32_e32 v7, 1, v4
	v_and_b32_e32 v3, 0xc0, v3
	v_and_or_b32 v5, v4, s0, v5
	v_and_b32_e32 v6, 4, v6
	v_and_b32_e32 v7, 24, v7
	v_sub_u32_e32 v2, v2, v3
	v_or3_b32 v5, v5, v6, v7
	v_lshlrev_b32_e32 v6, 5, v10
	v_ashrrev_i16_sdwa v2, v197, sext(v2) dst_sel:DWORD dst_unused:UNUSED_PAD src0_sel:DWORD src1_sel:BYTE_0
	v_and_b32_e32 v6, 32, v6
	v_bfe_i32 v12, v2, 0, 16
	v_add_lshl_u32 v2, v6, v12, 1
	v_lshl_add_u32 v130, v5, 11, v2
	v_lshl_add_u32 v132, v4, 11, v2
	v_bfe_i32 v2, v16, 27, 1
	v_lshrrev_b32_e32 v2, 22, v2
	v_add_u32_e32 v2, v1, v2
	v_and_b32_e32 v2, 0xfffffc00, v2
	v_sub_u32_e32 v1, v1, v2
	v_lshrrev_b32_e32 v2, 4, v1
	v_ashrrev_i32_e32 v3, 31, v16
	v_bitop3_b32 v1, v2, v1, 32 bitop3:0x6c
	v_lshrrev_b32_e32 v3, 26, v3
	v_ashrrev_i32_e32 v2, 31, v1
	v_add_u32_e32 v3, v16, v3
	v_lshrrev_b32_e32 v2, 26, v2
	v_ashrrev_i32_e32 v14, 6, v3
	v_add_u32_e32 v2, v1, v2
	v_lshlrev_b32_e32 v3, 3, v14
	v_ashrrev_i32_e32 v13, 6, v2
	v_and_b32_e32 v3, -16, v3
	v_add_u32_e32 v3, v13, v3
	v_and_b32_e32 v4, 3, v13
	v_lshrrev_b32_e32 v5, 2, v3
	v_lshlrev_b32_e32 v6, 1, v3
	v_and_b32_e32 v2, 0xc0, v2
	s_addc_u32 s43, s1, 0
	s_ashr_i32 s5, s4, 6
	v_and_or_b32 v4, v3, s0, v4
	v_and_b32_e32 v5, 4, v5
	v_and_b32_e32 v6, 24, v6
	v_sub_u32_e32 v1, v1, v2
	s_ashr_i32 s12, s4, 8
	s_lshl_b32 s44, s5, 10
	v_or3_b32 v4, v4, v5, v6
	v_lshlrev_b32_e32 v5, 5, v14
	v_ashrrev_i16_sdwa v1, v197, sext(v1) dst_sel:DWORD dst_unused:UNUSED_PAD src0_sel:DWORD src1_sel:BYTE_0
	v_readlane_b32 s0, v254, 44
	v_and_b32_e32 v5, 32, v5
	v_bfe_i32 v15, v1, 0, 16
	v_readlane_b32 s1, v254, 45
	s_add_u32 s18, s42, s0
	v_add_lshl_u32 v1, v5, v15, 1
	s_addc_u32 s19, s43, s1
	s_add_i32 s45, s44, 0
	v_lshl_add_u32 v162, v4, 11, v1
	s_add_i32 m0, s45, 0x10000
	v_lshl_add_u32 v134, v3, 11, v1
	global_load_lds_dwordx4 v162, s[18:19]
	s_add_i32 m0, s45, 0x12000
	s_add_u32 s0, s18, 0x40000
	global_load_lds_dwordx4 v130, s[18:19]
	s_addc_u32 s1, s19, 0
	s_add_i32 m0, s45, 0x14000
	v_mov_b32_e32 v131, v163
	global_load_lds_dwordx4 v162, s[0:1]
	s_add_i32 m0, s45, 0x16000
	v_mov_b32_e32 v135, v163
	global_load_lds_dwordx4 v130, s[0:1]
	v_readlane_b32 s0, v254, 56
	v_readlane_b32 s1, v254, 57
	s_add_u32 s8, s11, s0
	s_addc_u32 s9, s16, s1
	s_add_i32 s46, s45, 0x2000
	s_mov_b32 m0, s45
	s_add_u32 s0, s8, 0x40000
	global_load_lds_dwordx4 v134, s[8:9]
	s_mov_b32 m0, s46
	s_addc_u32 s1, s9, 0
	s_add_i32 s47, s45, 0x4000
	global_load_lds_dwordx4 v132, s[8:9]
	s_mov_b32 m0, s47
	s_add_i32 s48, s45, 0x6000
	global_load_lds_dwordx4 v134, s[0:1]
	s_mov_b32 m0, s48
	v_mov_b32_e32 v133, v163
	global_load_lds_dwordx4 v132, s[0:1]
	s_cmp_eq_u32 s12, 1
	v_lshl_add_u64 v[8:9], s[18:19], 0, v[162:163]
	v_lshl_add_u64 v[6:7], s[18:19], 0, v[130:131]
	v_lshl_add_u64 v[2:3], s[8:9], 0, v[134:135]
	s_cselect_b64 s[0:1], -1, 0
	s_cmp_lg_u32 s12, 1
	v_lshl_add_u64 v[4:5], s[8:9], 0, v[132:133]
	s_cbranch_scc1 .LBB0_1046
	s_barrier
